# output bias prefetched in the prologue into spare VGPRs (nfv 256, still 2 waves/SIMD); epilogue no longer waits on bias loads
# baseline (speedup 1.0000x reference)
_Z7k_fusedPKDF16_S0_S0_S0_PKfS2_S2_Pf:
	v_lshrrev_b32_e32 v222, 6, v0
	v_and_b32_e32 v1, 63, v0
	s_load_dwordx8 s[24:31], s[0:1], 0x8
	s_load_dwordx4 s[36:39], s[0:1], 0x28
	v_lshlrev_b32_e32 v4, 2, v222
	v_lshlrev_b32_e32 v5, 3, v1
	v_lshl_or_b32 v2, v222, 11, v5
	v_lshlrev_b32_e32 v224, 12, v222
	v_or_b32_e32 v6, 1, v4
	v_lshlrev_b32_e32 v223, 1, v2
	v_readfirstlane_b32 s3, v224
	v_lshl_or_b32 v2, v6, 9, v5
	v_lshlrev_b32_e32 v225, 10, v6
	v_mov_b32_e32 v211, 0
	s_mov_b32 m0, s3
	v_lshlrev_b32_e32 v210, 1, v2
	v_readfirstlane_b32 s3, v225
	s_waitcnt lgkmcnt(0)
	global_load_lds_dwordx4 v223, s[24:25]
	v_lshl_add_u64 v[2:3], s[24:25], 0, v[210:211]
	s_mov_b32 m0, s3
	v_or_b32_e32 v6, 2, v4
	global_load_lds_dwordx4 v[2:3], off
	v_lshl_or_b32 v2, v6, 9, v5
	v_lshlrev_b32_e32 v212, 1, v2
	v_mov_b32_e32 v213, v211
	v_lshl_add_u64 v[2:3], s[24:25], 0, v[212:213]
	v_lshlrev_b32_e32 v213, 10, v6
	v_or_b32_e32 v4, 3, v4
	v_readfirstlane_b32 s3, v213
	s_mov_b32 m0, s3
	v_mov_b32_e32 v215, v211
	global_load_lds_dwordx4 v[2:3], off
	v_lshl_or_b32 v2, v4, 9, v5
	v_lshlrev_b32_e32 v214, 1, v2
	v_lshl_add_u64 v[2:3], s[24:25], 0, v[214:215]
	v_lshlrev_b32_e32 v215, 10, v4
	s_nop 0
	v_readfirstlane_b32 s3, v215
	s_mov_b32 m0, s3
	s_movk_i32 s3, 0xff
	global_load_lds_dwordx4 v[2:3], off
	v_and_b32_e32 v2, 0x7f, v0
	v_lshlrev_b32_e32 v2, 2, v2
	global_load_dword v4, v2, s[36:37]
	global_load_dword v5, v2, s[38:39]
	v_and_b32_e32 v252, 31, v0
	v_lshlrev_b32_e32 v252, 2, v252
	global_load_dword v248, v252, s[38:39]
	global_load_dword v249, v252, s[38:39] offset:128
	global_load_dword v250, v252, s[38:39] offset:256
	global_load_dword v251, v252, s[38:39] offset:384
	s_lshl_b32 s3, s2, 8
	s_load_dwordx2 s[4:5], s[0:1], 0x0
	v_and_b32_e32 v6, 0xff, v0
	v_or_b32_e32 v6, s3, v6
	v_ashrrev_i32_e32 v7, 31, v6
	v_lshl_add_u64 v[6:7], v[6:7], 2, s[30:31]
	global_load_dword v244, v[6:7], off
	v_mov_b32_e32 v208, s3
	v_lshl_or_b32 v2, s2, 3, v222
	v_ashrrev_i32_e32 v3, 31, v2
	v_lshlrev_b64 v[2:3], 13, v[2:3]
	s_waitcnt lgkmcnt(0)
	v_lshl_add_u64 v[6:7], s[4:5], 0, v[2:3]
	v_mov_b32_e32 v2, 0
	v_lshlrev_b32_e32 v206, 4, v1
	v_mov_b32_e32 v207, v2
	v_lshl_add_u64 v[6:7], v[6:7], 0, v[206:207]
	v_lshlrev_b32_e32 v211, 13, v222
	v_ashrrev_i32_e32 v209, 31, v208
	v_lshl_add_u64 v[8:9], v[208:209], 2, s[30:31]
	v_or_b32_e32 v3, v211, v206
	v_lshl_add_u64 v[8:9], v[8:9], 0, v[206:207]
	global_load_dwordx4 v[68:71], v[8:9], off
	global_load_dwordx4 v[130:133], v[6:7], off
	global_load_dwordx4 v[134:137], v[6:7], off offset:1024
	global_load_dwordx4 v[138:141], v[6:7], off offset:2048
	global_load_dwordx4 v[142:145], v[6:7], off offset:3072
	s_movk_i32 s33, 0x1000
	v_add_co_u32_e32 v14, vcc, s33, v6
	s_nop 1
	v_addc_co_u32_e32 v15, vcc, 0, v7, vcc
	global_load_dwordx4 v[146:149], v[14:15], off
	global_load_dwordx4 v[150:153], v[14:15], off offset:1024
	global_load_dwordx4 v[154:157], v[14:15], off offset:2048
	global_load_dwordx4 v[158:161], v[14:15], off offset:3072
	v_lshlrev_b32_e32 v10, 1, v3
	global_load_dwordx4 v[186:189], v10, s[28:29] offset:16
	global_load_dwordx4 v[190:193], v10, s[28:29]
	global_load_dwordx4 v[178:181], v10, s[28:29] offset:2064
	global_load_dwordx4 v[182:185], v10, s[28:29] offset:2048
	v_mov_b32_e32 v11, v2
	v_lshl_add_u64 v[8:9], s[28:29], 0, v[10:11]
	v_add_co_u32_e32 v12, vcc, s33, v8
	s_mov_b64 s[34:35], 0x1000
	s_nop 0
	v_addc_co_u32_e32 v13, vcc, 0, v9, vcc
	s_mov_b64 s[40:41], 0x1800
	v_lshl_add_u64 v[10:11], v[8:9], 0, s[34:35]
	v_lshl_add_u64 v[8:9], v[8:9], 0, s[40:41]
	global_load_dwordx4 v[170:173], v[12:13], off
	global_load_dwordx4 v[174:177], v[10:11], off offset:16
	global_load_dwordx4 v[162:165], v[12:13], off offset:2048
	global_load_dwordx4 v[166:169], v[8:9], off offset:16
	s_waitcnt vmcnt(17)
	v_cmp_gt_u32_e32 vcc, 0x100, v0
	s_and_saveexec_b64 s[4:5], vcc
	v_lshlrev_b32_e32 v12, 4, v0
	v_and_b32_e32 v13, 0xe3, v0
	v_lshlrev_b32_e32 v14, 1, v0
	v_and_b32_e32 v12, 64, v12
	s_mov_b32 s8, 0x20000
	v_and_b32_e32 v14, 48, v14
	v_lshl_or_b32 v13, v13, 2, v12
	v_or3_b32 v13, v13, v14, s8
	v_add_f32_e32 v12, -1.0, v244
	v_mul_f32_e32 v12, 0x47000000, v12
	v_mul_f32_e32 v12, 0x3fb8aa3b, v12
	ds_write_b32 v13, v12
	s_or_b64 exec, exec, s[4:5]
	s_waitcnt lgkmcnt(0)
	s_barrier
	ds_read_b128 v[4:7], v206 offset:8192
	ds_read_b128 v[72:75], v206 offset:9216
	s_load_dwordx2 s[30:31], s[0:1], 0x38
	s_mov_b32 s0, 0x47000000
	s_mov_b32 s42, 0x3fb8aa3b
	s_mov_b32 s43, 0xff800000
	v_lshrrev_b32_e32 v96, 5, v1
	v_lshlrev_b32_e32 v97, 4, v96
	v_lshl_or_b32 v209, v222, 11, v206
	v_lshlrev_b32_e32 v1, 5, v1
	s_add_u32 s54, s24, 0x8000
	v_lshlrev_b32_e32 v207, 2, v96
	s_addc_u32 s55, s25, 0
	v_or_b32_e32 v227, 0x10000, v3
	s_mov_b32 s56, 0xc1d00000
	s_mov_b64 s[44:45], 0x20000
	s_mov_b64 s[46:47], 0x20800
	s_mov_b64 s[48:49], 0x21000
	s_mov_b32 s57, 0x21000
	s_mov_b64 s[50:51], 0x21800
	v_mov_b32_e32 v194, 0x3c003c00
	s_waitcnt lgkmcnt(0)
	s_waitcnt vmcnt(15)
	v_mfma_f32_32x32x16_f16 v[36:51], v[4:7], v[130:133], 0
	ds_read_b128 v[4:7], v206
	ds_read_b128 v[76:79], v206 offset:1024
	ds_read_b128 v[20:23], v206 offset:24576
	ds_read_b128 v[80:83], v206 offset:25600
	ds_read_b128 v[52:55], v206 offset:16384
	ds_read_b128 v[84:87], v206 offset:17408
	v_max_f32_e32 v71, v71, v71
	s_waitcnt lgkmcnt(1)
	v_mfma_f32_32x32x16_f16 v[52:67], v[130:133], v[52:55], 0
	v_max_f32_e32 v70, v70, v70
	v_max_f32_e32 v70, v70, v71
	s_waitcnt vmcnt(14)
	v_mfma_f32_32x32x16_f16 v[36:51], v[72:75], v[134:137], v[36:51]
	s_waitcnt lgkmcnt(0)
	v_mfma_f32_32x32x16_f16 v[52:67], v[134:137], v[84:87], v[52:67]
	ds_read_b128 v[72:75], v206 offset:10240
	ds_read_b128 v[84:87], v206 offset:11264
	s_waitcnt lgkmcnt(1)
	s_waitcnt vmcnt(13)
	v_mfma_f32_32x32x16_f16 v[36:51], v[72:75], v[138:141], v[36:51]
	ds_read_b128 v[72:75], v206 offset:18432
	ds_read_b128 v[88:91], v206 offset:19456
	s_waitcnt lgkmcnt(1)
	v_mfma_f32_32x32x16_f16 v[52:67], v[138:141], v[72:75], v[52:67]
	ds_read_b128 v[72:75], v206 offset:12288
	s_waitcnt vmcnt(12)
	v_mfma_f32_32x32x16_f16 v[36:51], v[84:87], v[142:145], v[36:51]
	v_mbcnt_lo_u32_b32 v84, -1, 0
	v_mbcnt_hi_u32_b32 v92, -1, v84
	ds_read_b128 v[84:87], v206 offset:13312
	v_xor_b32_e32 v93, 1, v92
	v_xor_b32_e32 v94, 2, v92
	v_xor_b32_e32 v95, 4, v92
	s_waitcnt lgkmcnt(2)
	v_mfma_f32_32x32x16_f16 v[52:67], v[142:145], v[88:91], v[52:67]
	v_and_b32_e32 v88, 64, v92
	v_add_u32_e32 v98, 64, v88
	v_cmp_lt_i32_e32 vcc, v93, v98
	ds_read_b128 v[88:91], v206 offset:21504
	s_waitcnt lgkmcnt(2)
	s_waitcnt vmcnt(11)
	v_mfma_f32_32x32x16_f16 v[36:51], v[72:75], v[146:149], v[36:51]
	ds_read_b128 v[72:75], v206 offset:20480
	s_waitcnt lgkmcnt(0)
	v_mfma_f32_32x32x16_f16 v[52:67], v[146:149], v[72:75], v[52:67]
	v_cndmask_b32_e32 v72, v92, v93, vcc
	v_lshlrev_b32_e32 v72, 2, v72
	v_max3_f32 v73, v68, v69, v70
	ds_bpermute_b32 v72, v72, v73
	v_cmp_lt_i32_e32 vcc, v94, v98
	s_waitcnt lgkmcnt(0)
	v_max_f32_e32 v72, v72, v72
	v_cndmask_b32_e32 v68, v92, v94, vcc
	v_lshlrev_b32_e32 v74, 2, v68
	ds_read_b128 v[68:71], v206 offset:14336
	s_waitcnt vmcnt(10)
	v_mfma_f32_32x32x16_f16 v[36:51], v[84:87], v[150:153], v[36:51]
	v_max_f32_e32 v84, v73, v72
	ds_bpermute_b32 v85, v74, v84
	v_cmp_lt_i32_e32 vcc, v95, v98
	s_waitcnt lgkmcnt(0)
	v_max_f32_e32 v85, v85, v85
	v_mfma_f32_32x32x16_f16 v[52:67], v[150:153], v[88:91], v[52:67]
	v_cndmask_b32_e32 v72, v92, v95, vcc
	v_lshlrev_b32_e32 v86, 2, v72
	v_max_f32_e32 v92, v84, v85
	ds_read_b128 v[72:75], v206 offset:15360
	ds_bpermute_b32 v93, v86, v92
	s_waitcnt lgkmcnt(0)
	v_max_f32_e32 v93, v93, v93
	s_waitcnt vmcnt(9)
	v_mfma_f32_32x32x16_f16 v[36:51], v[68:71], v[154:157], v[36:51]
	ds_read_b128 v[68:71], v206 offset:22528
	ds_read_b128 v[84:87], v206 offset:23552
	v_max_f32_e32 v92, v92, v93
	global_load_dwordx4 v[88:91], v97, s[36:37]
	v_readlane_b32 s3, v92, 0
	v_readlane_b32 s2, v92, 8
	v_readlane_b32 s5, v92, 16
	v_readlane_b32 s4, v92, 24
	s_waitcnt lgkmcnt(1)
	v_mfma_f32_32x32x16_f16 v[52:67], v[154:157], v[68:71], v[52:67]
	v_add_f32_e64 v68, s2, -1.0
	v_add_f32_e64 v69, s3, -1.0
	v_readlane_b32 s7, v92, 32
	v_readlane_b32 s6, v92, 40
	v_add_f32_e64 v70, s4, -1.0
	v_add_f32_e64 v71, s5, -1.0
	v_pk_mul_f32 v[68:69], v[68:69], s[0:1] op_sel_hi:[1,0]
	v_readlane_b32 s9, v92, 48
	v_readlane_b32 s8, v92, 56
	v_mfma_f32_32x32x16_f16 v[20:35], v[20:23], v[130:133], 0
	v_mul_f32_e64 v70, v70, s0
	v_mul_f32_e64 v71, v71, s0
	v_mul_f32_e64 v92, v68, s42
	v_mul_f32_e64 v93, v69, s42
	v_mul_f32_e64 v94, v70, s42
	v_mul_f32_e64 v95, v71, s42
	v_max3_f32 v68, v93, s43, v92
	v_max3_f32 v68, v68, v95, v94
	s_waitcnt vmcnt(9)
	v_mfma_f32_32x32x16_f16 v[36:51], v[72:75], v[158:161], v[36:51]
	v_add_f32_e64 v72, s6, -1.0
	v_add_f32_e64 v73, s7, -1.0
	v_mul_f32_e64 v72, v72, s0
	v_mul_f32_e64 v73, v73, s0
	s_waitcnt lgkmcnt(0)
	v_mfma_f32_32x32x16_f16 v[52:67], v[158:161], v[84:87], v[52:67]
	v_mul_f32_e64 v84, v72, s42
	v_mul_f32_e64 v85, v73, s42
	v_add_f32_e64 v86, s8, -1.0
	v_add_f32_e64 v87, s9, -1.0
	v_max3_f32 v98, v68, v85, v84
	ds_read_b128 v[68:71], v206 offset:26624
	v_cvt_pk_f16_f32 v43, v42, v43
	v_cvt_pk_f16_f32 v42, v40, v41
	v_cvt_pk_f16_f32 v41, v38, v39
	v_mfma_f32_32x32x16_f16 v[20:35], v[80:83], v[134:137], v[20:35]
	v_mul_f32_e64 v80, v86, s0
	v_mul_f32_e64 v81, v87, s0
	v_cvt_pk_f16_f32 v40, v36, v37
	v_mul_f32_e64 v86, v80, s42
	v_mul_f32_e64 v87, v81, s42
	global_load_dwordx4 v[72:75], v97, s[36:37] offset:32
	v_max3_f32 v80, v98, v87, v86
	v_add_f32_e32 v98, 0xc53b8000, v80
	ds_read_b128 v[80:83], v206 offset:27648
	global_load_dwordx4 v[36:39], v97, s[36:37] offset:64
	ds_write_b128 v209, v[40:43] offset:32768
	v_cvt_pk_f16_f32 v43, v50, v51
	v_cvt_pk_f16_f32 v40, v44, v45
	v_cvt_pk_f16_f32 v44, v52, v53
	global_load_dwordx4 v[50:53], v97, s[36:37] offset:96
	s_waitcnt lgkmcnt(2)
	v_mfma_f32_32x32x16_f16 v[20:35], v[68:71], v[138:141], v[20:35]
	ds_read_b128 v[68:71], v206 offset:28672
	v_cvt_pk_f16_f32 v42, v48, v49
	v_cvt_pk_f16_f32 v41, v46, v47
	ds_write_b128 v209, v[40:43] offset:33792
	ds_read_b128 v[40:43], v206 offset:30720
	v_cvt_pk_f16_f32 v47, v58, v59
	v_cvt_pk_f16_f32 v46, v56, v57
	s_waitcnt lgkmcnt(4)
	v_mfma_f32_32x32x16_f16 v[20:35], v[80:83], v[142:145], v[20:35]
	ds_read_b128 v[80:83], v206 offset:29696
	v_cvt_pk_f16_f32 v45, v54, v55
	ds_write_b128 v209, v[44:47] offset:49152
	v_cvt_pk_f16_f32 v45, v66, v67
	ds_read_b128 v[46:49], v206 offset:31744
	v_cvt_pk_f16_f32 v44, v64, v65
	v_cmp_ge_f32_e64 s[0:1], v92, v98
	s_waitcnt lgkmcnt(5)
	v_mfma_f32_32x32x16_f16 v[20:35], v[68:71], v[146:149], v[20:35]
	v_cmp_ge_f32_e64 s[2:3], v93, v98
	v_cmp_ge_f32_e64 s[4:5], v94, v98
	v_cmp_ge_f32_e64 s[6:7], v95, v98
	v_cmp_ge_f32_e64 s[8:9], v84, v98
	v_cmp_ge_f32_e64 s[10:11], v85, v98
	v_cmp_ge_f32_e64 s[12:13], v86, v98
	v_cmp_ge_f32_e64 s[14:15], v87, v98
	v_mfma_f32_32x32x16_f16 v[4:19], v[4:7], v[130:133], 0
	s_waitcnt lgkmcnt(2)
	v_mfma_f32_32x32x16_f16 v[20:35], v[80:83], v[150:153], v[20:35]
	v_mfma_f32_32x32x16_f16 v[4:19], v[76:79], v[134:137], v[4:19]
	v_mfma_f32_32x32x16_f16 v[20:35], v[40:43], v[154:157], v[20:35]
	v_cvt_pk_f16_f32 v43, v62, v63
	v_cvt_pk_f16_f32 v42, v60, v61
	ds_write_b128 v209, v[42:45] offset:50176
	ds_read_b128 v[40:43], v206 offset:2048
	ds_read_b128 v[54:57], v206 offset:3072
	s_waitcnt lgkmcnt(1)
	v_mfma_f32_32x32x16_f16 v[4:19], v[40:43], v[138:141], v[4:19]
	s_waitcnt lgkmcnt(0)
	v_mfma_f32_32x32x16_f16 v[4:19], v[54:57], v[142:145], v[4:19]
	v_mfma_f32_32x32x16_f16 v[20:35], v[46:49], v[158:161], v[20:35]
	ds_read_b128 v[44:47], v206 offset:4096
	ds_read_b128 v[58:61], v206 offset:5120
	ds_read_b128 v[62:65], v206 offset:6144
	ds_read_b128 v[66:69], v206 offset:7168
	s_waitcnt lgkmcnt(0)
	s_barrier
	s_waitcnt vmcnt(3)
	s_nop 4
	v_add_f32_e32 v20, v20, v88
	v_mfma_f32_32x32x16_f16 v[4:19], v[44:47], v[146:149], v[4:19]
	v_add_f32_e32 v21, v89, v21
	v_add_f32_e32 v22, v90, v22
	v_add_f32_e32 v23, v91, v23
	s_waitcnt vmcnt(2)
	v_add_f32_e32 v24, v24, v72
	v_add_f32_e32 v25, v73, v25
	v_add_f32_e32 v26, v74, v26
	v_add_f32_e32 v27, v75, v27
	v_mfma_f32_32x32x16_f16 v[4:19], v[58:61], v[150:153], v[4:19]
	s_waitcnt vmcnt(1)
	v_add_f32_e32 v28, v28, v36
	v_add_f32_e32 v29, v37, v29
	v_add_f32_e32 v30, v38, v30
	v_add_f32_e32 v31, v39, v31
	s_waitcnt vmcnt(0)
	v_add_f32_e32 v32, v32, v50
	v_add_f32_e32 v33, v51, v33
	v_add_f32_e32 v34, v52, v34
	v_mfma_f32_32x32x16_f16 v[4:19], v[62:65], v[154:157], v[4:19]
	v_add_f32_e32 v35, v53, v35
	v_mul_f32_e32 v20, 0xbfb8aa3b, v20
	v_mul_f32_e32 v21, 0xbfb8aa3b, v21
	v_mul_f32_e32 v22, 0xbfb8aa3b, v22
	v_mul_f32_e32 v23, 0xbfb8aa3b, v23
	v_mul_f32_e32 v24, 0xbfb8aa3b, v24
	v_mul_f32_e32 v25, 0xbfb8aa3b, v25
	v_mfma_f32_32x32x16_f16 v[4:19], v[66:69], v[158:161], v[4:19]
	v_mul_f32_e32 v26, 0xbfb8aa3b, v26
	v_mul_f32_e32 v27, 0xbfb8aa3b, v27
	v_mul_f32_e32 v28, 0xbfb8aa3b, v28
	v_mul_f32_e32 v29, 0xbfb8aa3b, v29
	v_mul_f32_e32 v30, 0xbfb8aa3b, v30
	v_mul_f32_e32 v31, 0xbfb8aa3b, v31
	v_mul_f32_e32 v32, 0xbfb8aa3b, v32
	v_mul_f32_e32 v33, 0xbfb8aa3b, v33
	v_mul_f32_e32 v34, 0xbfb8aa3b, v34
	v_mul_f32_e32 v35, 0xbfb8aa3b, v35
	v_exp_f32_e32 v20, v20
	v_exp_f32_e32 v21, v21
	v_exp_f32_e32 v22, v22
	v_exp_f32_e32 v23, v23
	v_exp_f32_e32 v24, v24
	v_exp_f32_e32 v25, v25
	v_exp_f32_e32 v26, v26
	v_exp_f32_e32 v27, v27
	v_exp_f32_e32 v28, v28
	v_exp_f32_e32 v29, v29
	v_exp_f32_e32 v30, v30
	v_exp_f32_e32 v31, v31
	v_exp_f32_e32 v32, v32
	v_exp_f32_e32 v33, v33
	v_exp_f32_e32 v34, v34
	v_exp_f32_e32 v35, v35
	v_add_f32_e32 v20, 1.0, v20
	v_add_f32_e32 v21, 1.0, v21
	v_add_f32_e32 v22, 1.0, v22
	v_add_f32_e32 v23, 1.0, v23
	v_add_f32_e32 v24, 1.0, v24
	v_add_f32_e32 v25, 1.0, v25
	v_add_f32_e32 v26, 1.0, v26
	v_add_f32_e32 v27, 1.0, v27
	v_add_f32_e32 v28, 1.0, v28
	v_add_f32_e32 v29, 1.0, v29
	v_add_f32_e32 v30, 1.0, v30
	v_add_f32_e32 v31, 1.0, v31
	v_add_f32_e32 v32, 1.0, v32
	v_add_f32_e32 v33, 1.0, v33
	v_add_f32_e32 v34, 1.0, v34
	v_add_f32_e32 v35, 1.0, v35
	v_rcp_f32_e32 v20, v20
	v_rcp_f32_e32 v21, v21
	v_rcp_f32_e32 v22, v22
	v_rcp_f32_e32 v23, v23
	v_rcp_f32_e32 v24, v24
	v_rcp_f32_e32 v25, v25
	v_rcp_f32_e32 v26, v26
	v_rcp_f32_e32 v27, v27
	v_rcp_f32_e32 v28, v28
	v_rcp_f32_e32 v29, v29
	v_rcp_f32_e32 v30, v30
	v_rcp_f32_e32 v31, v31
	v_rcp_f32_e32 v32, v32
	v_rcp_f32_e32 v33, v33
	v_rcp_f32_e32 v34, v34
	v_rcp_f32_e32 v35, v35
	v_cvt_pk_f16_f32 v198, v4, v5
	v_lshl_or_b32 v4, v222, 14, v1
	v_mov_b32_e32 v5, v2
	v_lshl_add_u64 v[216:217], s[28:29], 0, v[4:5]
	v_or_b32_e32 v4, 0x2000, v4
	v_lshrrev_b32_e32 v1, 1, v0
	v_lshl_add_u64 v[218:219], s[28:29], 0, v[4:5]
	v_and_b32_e32 v4, 16, v1
	v_mov_b32_e32 v36, 0x20000
	v_lshl_add_u64 v[4:5], s[36:37], 0, v[4:5]
	s_mov_b64 s[28:29], 0x80
	v_lshl_or_b32 v226, v96, 6, v36
	v_cvt_pk_f16_f32 v199, v6, v7
	v_cvt_pk_f16_f32 v200, v8, v9
	v_cvt_pk_f16_f32 v201, v10, v11
	v_cvt_pk_f16_f32 v202, v12, v13
	v_cvt_pk_f16_f32 v203, v14, v15
	v_cvt_pk_f16_f32 v204, v16, v17
	v_cvt_pk_f16_f32 v205, v18, v19
	v_cvt_pk_f16_f32 v229, v20, v21
	v_cvt_pk_f16_f32 v230, v22, v23
	v_cvt_pk_f16_f32 v232, v24, v25
	v_cvt_pk_f16_f32 v234, v26, v27
	v_cvt_pk_f16_f32 v228, v28, v29
	v_cvt_pk_f16_f32 v231, v30, v31
	v_cvt_pk_f16_f32 v233, v32, v33
	v_cvt_pk_f16_f32 v235, v34, v35
	v_lshl_add_u64 v[220:221], v[4:5], 0, s[28:29]
	s_mov_b64 s[36:37], 0
	s_branch .LBB1_6

.LBB1_90:
	v_and_b32_e32 v0, 31, v0
	v_lshlrev_b32_e32 v50, 2, v0
	v_mov_b32_e32 v0, v248
	v_mov_b32_e32 v16, v249
	v_mov_b32_e32 v32, v250
	s_mov_b32 s0, 0x10000
	v_add3_u32 v49, v206, v211, s0
	ds_read_b128 v[34:37], v206
	ds_read_b128 v[42:45], v206 offset:1024
	ds_read_b128 v[52:55], v206 offset:2048
	ds_read_b128 v[64:67], v206 offset:3072
	ds_read_b128 v[38:41], v49
	ds_read_b128 v[56:59], v49
	v_mov_b32_e32 v48, v251
	v_lshl_add_u32 v120, v222, 5, v208
	v_or_b32_e32 v136, v120, v207
	v_mov_b32_e32 v51, 0
	v_lshl_add_u64 v[138:139], s[30:31], 0, v[50:51]
	v_ashrrev_i32_e32 v137, 31, v136
	v_or_b32_e32 v50, 1, v136
	v_or_b32_e32 v140, 2, v136
	v_or_b32_e32 v142, 3, v136
	v_or_b32_e32 v144, 8, v136
	v_or_b32_e32 v146, 9, v136
	v_lshlrev_b64 v[150:151], 9, v[136:137]
	v_ashrrev_i32_e32 v51, 31, v50
	v_ashrrev_i32_e32 v141, 31, v140
	v_ashrrev_i32_e32 v143, 31, v142
	v_ashrrev_i32_e32 v145, 31, v144
	v_ashrrev_i32_e32 v147, 31, v146
	v_lshl_add_u64 v[150:151], v[138:139], 0, v[150:151]
	v_lshlrev_b64 v[50:51], 9, v[50:51]
	v_or_b32_e32 v148, 10, v136
	v_ashrrev_i32_e32 v149, 31, v148
	s_waitcnt vmcnt(3)
	v_mov_b32_e32 v1, v0
	v_mov_b32_e32 v2, v0
	v_mov_b32_e32 v3, v0
	v_mov_b32_e32 v4, v0
	v_mov_b32_e32 v5, v0
	v_mov_b32_e32 v6, v0
	v_mov_b32_e32 v7, v0
	v_mov_b32_e32 v8, v0
	v_mov_b32_e32 v9, v0
	v_mov_b32_e32 v10, v0
	v_mov_b32_e32 v11, v0
	v_mov_b32_e32 v12, v0
	v_mov_b32_e32 v13, v0
	v_mov_b32_e32 v14, v0
	v_mov_b32_e32 v15, v0
	s_waitcnt vmcnt(2)
	v_mov_b32_e32 v17, v16
	v_mov_b32_e32 v18, v16
	s_waitcnt lgkmcnt(1)
	v_mfma_f32_32x32x16_f16 v[0:15], v[38:41], v[34:37], v[0:15]
	v_mov_b32_e32 v19, v16
	v_mov_b32_e32 v20, v16
	v_mov_b32_e32 v21, v16
	v_mov_b32_e32 v22, v16
	v_mov_b32_e32 v23, v16
	v_mov_b32_e32 v24, v16
	v_mov_b32_e32 v25, v16
	v_mov_b32_e32 v26, v16
	v_mov_b32_e32 v27, v16
	v_mov_b32_e32 v28, v16
	v_mov_b32_e32 v29, v16
	v_mov_b32_e32 v30, v16
	v_mov_b32_e32 v31, v16
	s_waitcnt vmcnt(1)
	v_mov_b32_e32 v33, v32
	v_mov_b32_e32 v34, v32
	v_mov_b32_e32 v35, v32
	v_mov_b32_e32 v36, v32
	v_mov_b32_e32 v37, v32
	v_mov_b32_e32 v38, v32
	v_mov_b32_e32 v39, v32
	v_mov_b32_e32 v40, v32
	s_waitcnt lgkmcnt(0)
	v_mfma_f32_32x32x16_f16 v[16:31], v[56:59], v[42:45], v[16:31]
	v_mov_b32_e32 v41, v32
	v_mov_b32_e32 v42, v32
	v_mov_b32_e32 v43, v32
	v_mov_b32_e32 v44, v32
	v_mov_b32_e32 v45, v32
	v_mov_b32_e32 v46, v32
	v_mov_b32_e32 v47, v32
	s_nop 1
	v_mfma_f32_32x32x16_f16 v[32:47], v[56:59], v[52:55], v[32:47]
	ds_read_b128 v[52:55], v49 offset:1024
	ds_read_b128 v[56:59], v206 offset:4096
	ds_read_b128 v[60:63], v206 offset:5120
	ds_read_b128 v[68:71], v49
	s_waitcnt lgkmcnt(2)
	v_mfma_f32_32x32x16_f16 v[0:15], v[52:55], v[56:59], v[0:15]
	ds_read_b128 v[52:55], v49 offset:1024
	ds_read_b128 v[72:75], v49 offset:1024
	s_waitcnt lgkmcnt(1)
	v_mfma_f32_32x32x16_f16 v[16:31], v[52:55], v[60:63], v[16:31]
	ds_read_b128 v[56:59], v49 offset:2048
	ds_read_b128 v[60:63], v206 offset:8192
	ds_read_b128 v[76:79], v206 offset:9216
	ds_read_b128 v[80:83], v49 offset:2048
	s_waitcnt lgkmcnt(2)
	v_mfma_f32_32x32x16_f16 v[0:15], v[56:59], v[60:63], v[0:15]
	s_waitcnt lgkmcnt(0)
	v_mfma_f32_32x32x16_f16 v[16:31], v[80:83], v[76:79], v[16:31]
	ds_read_b128 v[56:59], v49 offset:3072
	ds_read_b128 v[60:63], v206 offset:12288
	ds_read_b128 v[76:79], v206 offset:13312
	ds_read_b128 v[84:87], v49 offset:2048
	s_waitcnt lgkmcnt(2)
	v_mfma_f32_32x32x16_f16 v[0:15], v[56:59], v[60:63], v[0:15]
	ds_read_b128 v[56:59], v49 offset:3072
	ds_read_b128 v[88:91], v49 offset:3072
	s_waitcnt lgkmcnt(1)
	v_mfma_f32_32x32x16_f16 v[16:31], v[56:59], v[76:79], v[16:31]
	ds_read_b128 v[60:63], v49 offset:4096
	ds_read_b128 v[76:79], v206 offset:16384
	ds_read_b128 v[92:95], v206 offset:17408
	ds_read_b128 v[96:99], v49 offset:4096
	s_waitcnt lgkmcnt(2)
	v_mfma_f32_32x32x16_f16 v[0:15], v[60:63], v[76:79], v[0:15]
	ds_read_b128 v[60:63], v49 offset:5120
	s_waitcnt lgkmcnt(1)
	v_mfma_f32_32x32x16_f16 v[16:31], v[96:99], v[92:95], v[16:31]
	ds_read_b128 v[76:79], v206 offset:20480
	ds_read_b128 v[92:95], v206 offset:21504
	ds_read_b128 v[100:103], v206 offset:24576
	ds_read_b128 v[104:107], v206 offset:25600
	ds_read_b128 v[108:111], v49 offset:5120
	ds_read_b128 v[112:115], v49 offset:4096
	s_waitcnt lgkmcnt(5)
	v_mfma_f32_32x32x16_f16 v[0:15], v[60:63], v[76:79], v[0:15]
	ds_read_b128 v[60:63], v206 offset:28672
	ds_read_b128 v[76:79], v206 offset:29696
	ds_read_b128 v[116:119], v206 offset:6144
	ds_read_b128 v[120:123], v49 offset:6144
	ds_read_b128 v[124:127], v49 offset:5120
	s_waitcnt lgkmcnt(1)
	v_mfma_f32_32x32x16_f16 v[0:15], v[120:123], v[100:103], v[0:15]
	v_mfma_f32_32x32x16_f16 v[16:31], v[108:111], v[92:95], v[16:31]
	ds_read_b128 v[92:95], v49 offset:6144
	ds_read_b128 v[100:103], v49 offset:7168
	ds_read_b128 v[120:123], v49 offset:6144
	ds_read_b128 v[128:131], v49 offset:7168
	ds_read_b128 v[132:135], v49 offset:7168
	s_waitcnt vmcnt(0)
	v_mov_b32_e32 v49, v48
	s_waitcnt lgkmcnt(3)
	v_mfma_f32_32x32x16_f16 v[0:15], v[100:103], v[60:63], v[0:15]
	v_lshlrev_b64 v[60:61], 9, v[144:145]
	v_lshlrev_b64 v[62:63], 9, v[146:147]
	v_lshl_add_u64 v[146:147], v[138:139], 0, v[60:61]
	v_lshl_add_u64 v[152:153], v[138:139], 0, v[62:63]
	v_mov_b32_e32 v60, v48
	v_mov_b32_e32 v61, v48
	v_mov_b32_e32 v62, v48
	v_mfma_f32_32x32x16_f16 v[32:47], v[52:55], v[116:119], v[32:47]
	v_mov_b32_e32 v54, v48
	v_mov_b32_e32 v55, v48
	v_mov_b32_e32 v63, v48
	v_mfma_f32_32x32x16_f16 v[16:31], v[92:95], v[104:107], v[16:31]
	v_lshlrev_b64 v[104:105], 9, v[140:141]
	v_lshlrev_b64 v[106:107], 9, v[142:143]
	v_lshl_add_u64 v[140:141], v[138:139], 0, v[50:51]
	v_lshl_add_u64 v[142:143], v[138:139], 0, v[104:105]
	v_lshl_add_u64 v[144:145], v[138:139], 0, v[106:107]
	global_store_dword v[150:151], v0, off nt
	global_store_dword v[140:141], v1, off nt
	global_store_dword v[142:143], v2, off nt
	global_store_dword v[144:145], v3, off nt
	global_store_dword v[146:147], v4, off nt
	global_store_dword v[152:153], v5, off nt
	ds_read_b128 v[0:3], v206 offset:7168
	ds_read_b128 v[50:53], v206 offset:10240
	v_lshlrev_b64 v[4:5], 9, v[148:149]
	v_lshl_add_u64 v[116:117], v[138:139], 0, v[4:5]
	v_or_b32_e32 v4, 11, v136
	v_ashrrev_i32_e32 v5, 31, v4
	s_waitcnt lgkmcnt(0)
	v_mfma_f32_32x32x16_f16 v[32:47], v[80:83], v[50:53], v[32:47]
	v_lshlrev_b64 v[4:5], 9, v[4:5]
	v_lshl_add_u64 v[118:119], v[138:139], 0, v[4:5]
	v_or_b32_e32 v50, 16, v136
	global_store_dword v[116:117], v6, off nt
	global_store_dword v[118:119], v7, off nt
	ds_read_b128 v[4:7], v206 offset:14336
	v_ashrrev_i32_e32 v51, 31, v50
	v_mfma_f32_32x32x16_f16 v[16:31], v[128:131], v[76:79], v[16:31]
	ds_read_b128 v[76:79], v206 offset:11264
	v_lshlrev_b64 v[50:51], 9, v[50:51]
	v_lshl_add_u64 v[148:149], v[138:139], 0, v[50:51]
	v_or_b32_e32 v50, 17, v136
	v_ashrrev_i32_e32 v51, 31, v50
	v_lshlrev_b64 v[50:51], 9, v[50:51]
	v_lshl_add_u64 v[154:155], v[138:139], 0, v[50:51]
	s_waitcnt lgkmcnt(1)
	v_mfma_f32_32x32x16_f16 v[32:47], v[56:59], v[4:7], v[32:47]
	v_mov_b32_e32 v50, v48
	v_mov_b32_e32 v51, v48
	v_mov_b32_e32 v52, v48
	v_mov_b32_e32 v53, v48
	v_mov_b32_e32 v56, v48
	v_mov_b32_e32 v57, v48
	v_mov_b32_e32 v58, v48
	v_mov_b32_e32 v59, v48
	ds_read_b128 v[80:83], v206 offset:15360
	ds_read_b128 v[4:7], v206 offset:18432
	v_mfma_f32_32x32x16_f16 v[48:63], v[68:71], v[64:67], v[48:63]
	ds_read_b128 v[100:103], v206 offset:19456
	global_store_dword v[148:149], v8, off nt
	v_or_b32_e32 v8, 18, v136
	ds_read_b128 v[104:107], v206 offset:27648
	global_store_dword v[154:155], v9, off nt
	v_ashrrev_i32_e32 v9, 31, v8
	v_lshlrev_b64 v[8:9], 9, v[8:9]
	v_mfma_f32_32x32x16_f16 v[48:63], v[72:75], v[0:3], v[48:63]
	v_or_b32_e32 v0, 26, v136
	v_or_b32_e32 v2, 27, v136
	v_ashrrev_i32_e32 v1, 31, v0
	v_ashrrev_i32_e32 v3, 31, v2
	v_lshlrev_b64 v[0:1], 9, v[0:1]
	v_lshlrev_b64 v[2:3], 9, v[2:3]
	v_lshl_add_u64 v[0:1], v[138:139], 0, v[0:1]
	s_waitcnt lgkmcnt(4)
	v_mfma_f32_32x32x16_f16 v[48:63], v[84:87], v[76:79], v[48:63]
	v_lshl_add_u64 v[2:3], v[138:139], 0, v[2:3]
	global_store_dword v[0:1], v14, off nt
	s_waitcnt lgkmcnt(3)
	v_mfma_f32_32x32x16_f16 v[48:63], v[88:91], v[80:83], v[48:63]
	s_waitcnt lgkmcnt(2)
	v_mfma_f32_32x32x16_f16 v[32:47], v[96:99], v[4:7], v[32:47]
	ds_read_b128 v[4:7], v206 offset:22528
	ds_read_b128 v[96:99], v206 offset:23552
	s_waitcnt lgkmcnt(3)
	v_mfma_f32_32x32x16_f16 v[48:63], v[112:115], v[100:103], v[48:63]
	s_waitcnt lgkmcnt(1)
	v_mfma_f32_32x32x16_f16 v[32:47], v[108:111], v[4:7], v[32:47]
	ds_read_b128 v[4:7], v206 offset:26624
	v_lshl_add_u64 v[108:109], v[138:139], 0, v[8:9]
	v_or_b32_e32 v8, 19, v136
	v_ashrrev_i32_e32 v9, 31, v8
	v_lshlrev_b64 v[8:9], 9, v[8:9]
	global_store_dword v[108:109], v10, off nt
	s_waitcnt lgkmcnt(1)
	v_mfma_f32_32x32x16_f16 v[48:63], v[124:127], v[96:99], v[48:63]
	s_waitcnt lgkmcnt(0)
	v_mfma_f32_32x32x16_f16 v[32:47], v[92:95], v[4:7], v[32:47]
	ds_read_b128 v[4:7], v206 offset:30720
	v_lshl_add_u64 v[92:93], v[138:139], 0, v[8:9]
	v_or_b32_e32 v8, 24, v136
	v_ashrrev_i32_e32 v9, 31, v8
	global_store_dword v[92:93], v11, off nt
	v_lshlrev_b64 v[94:95], 9, v[8:9]
	ds_read_b128 v[8:11], v206 offset:31744
	v_mfma_f32_32x32x16_f16 v[48:63], v[120:123], v[104:107], v[48:63]
	s_waitcnt lgkmcnt(1)
	v_mfma_f32_32x32x16_f16 v[32:47], v[128:131], v[4:7], v[32:47]
	v_or_b32_e32 v6, 25, v136
	v_ashrrev_i32_e32 v7, 31, v6
	v_lshlrev_b64 v[6:7], 9, v[6:7]
	v_lshl_add_u64 v[4:5], v[138:139], 0, v[94:95]
	v_lshl_add_u64 v[6:7], v[138:139], 0, v[6:7]
	global_store_dword v[4:5], v12, off nt
	global_store_dword v[6:7], v13, off nt
	s_waitcnt lgkmcnt(0)
	v_mfma_f32_32x32x16_f16 v[48:63], v[132:135], v[8:11], v[48:63]
	global_store_dword v[2:3], v15, off nt
	global_store_dword v[150:151], v16, off offset:128 nt
	global_store_dword v[140:141], v17, off offset:128 nt
	global_store_dword v[142:143], v18, off offset:128 nt
	global_store_dword v[144:145], v19, off offset:128 nt
	global_store_dword v[146:147], v20, off offset:128 nt
	global_store_dword v[152:153], v21, off offset:128 nt
	global_store_dword v[116:117], v22, off offset:128 nt
	global_store_dword v[118:119], v23, off offset:128 nt
	global_store_dword v[148:149], v24, off offset:128 nt
	global_store_dword v[154:155], v25, off offset:128 nt
	global_store_dword v[108:109], v26, off offset:128 nt
	global_store_dword v[92:93], v27, off offset:128 nt
	global_store_dword v[4:5], v28, off offset:128 nt
	global_store_dword v[6:7], v29, off offset:128 nt
	global_store_dword v[0:1], v30, off offset:128 nt
	global_store_dword v[2:3], v31, off offset:128 nt
	global_store_dword v[150:151], v32, off offset:256 nt
	global_store_dword v[140:141], v33, off offset:256 nt
	global_store_dword v[142:143], v34, off offset:256 nt
	global_store_dword v[144:145], v35, off offset:256 nt
	global_store_dword v[146:147], v36, off offset:256 nt
	global_store_dword v[152:153], v37, off offset:256 nt
	global_store_dword v[116:117], v38, off offset:256 nt
	global_store_dword v[118:119], v39, off offset:256 nt
	global_store_dword v[148:149], v40, off offset:256 nt
	global_store_dword v[154:155], v41, off offset:256 nt
	global_store_dword v[108:109], v42, off offset:256 nt
	global_store_dword v[92:93], v43, off offset:256 nt
	global_store_dword v[4:5], v44, off offset:256 nt
	global_store_dword v[6:7], v45, off offset:256 nt
	global_store_dword v[0:1], v46, off offset:256 nt
	global_store_dword v[2:3], v47, off offset:256 nt
	global_store_dword v[150:151], v48, off offset:384 nt
	global_store_dword v[140:141], v49, off offset:384 nt
	global_store_dword v[142:143], v50, off offset:384 nt
	global_store_dword v[144:145], v51, off offset:384 nt
	global_store_dword v[146:147], v52, off offset:384 nt
	global_store_dword v[152:153], v53, off offset:384 nt
	global_store_dword v[116:117], v54, off offset:384 nt
	global_store_dword v[118:119], v55, off offset:384 nt
	global_store_dword v[148:149], v56, off offset:384 nt
	global_store_dword v[154:155], v57, off offset:384 nt
	global_store_dword v[108:109], v58, off offset:384 nt
	global_store_dword v[92:93], v59, off offset:384 nt
	global_store_dword v[4:5], v60, off offset:384 nt
	global_store_dword v[6:7], v61, off offset:384 nt
	global_store_dword v[0:1], v62, off offset:384 nt
	global_store_dword v[2:3], v63, off offset:384 nt
	s_endpgm

	.amdhsa_kernel _Z7k_fusedPKDF16_S0_S0_S0_PKfS2_S2_Pf
		.amdhsa_group_segment_fixed_size 132096
		.amdhsa_private_segment_fixed_size 0
		.amdhsa_kernarg_size 64
		.amdhsa_user_sgpr_count 2
		.amdhsa_user_sgpr_dispatch_ptr 0
		.amdhsa_user_sgpr_queue_ptr 0
		.amdhsa_user_sgpr_kernarg_segment_ptr 1
		.amdhsa_user_sgpr_dispatch_id 0
		.amdhsa_user_sgpr_kernarg_preload_length 0
		.amdhsa_user_sgpr_kernarg_preload_offset 0
		.amdhsa_user_sgpr_private_segment_size 0
		.amdhsa_uses_dynamic_stack 0
		.amdhsa_enable_private_segment 0
		.amdhsa_system_sgpr_workgroup_id_x 1
		.amdhsa_system_sgpr_workgroup_id_y 0
		.amdhsa_system_sgpr_workgroup_id_z 0
		.amdhsa_system_sgpr_workgroup_info 0
		.amdhsa_system_vgpr_workitem_id 0
		.amdhsa_next_free_vgpr 256
		.amdhsa_next_free_sgpr 96
		.amdhsa_accum_offset 256
		.amdhsa_reserve_vcc 1
		.amdhsa_float_round_mode_32 0
		.amdhsa_float_round_mode_16_64 0
		.amdhsa_float_denorm_mode_32 3
		.amdhsa_float_denorm_mode_16_64 3
		.amdhsa_dx10_clamp 1
		.amdhsa_ieee_mode 1
		.amdhsa_fp16_overflow 0
		.amdhsa_tg_split 0
		.amdhsa_exception_fp_ieee_invalid_op 0
		.amdhsa_exception_fp_denorm_src 0
		.amdhsa_exception_fp_ieee_div_zero 0
		.amdhsa_exception_fp_ieee_overflow 0
		.amdhsa_exception_fp_ieee_underflow 0
		.amdhsa_exception_fp_ieee_inexact 0
		.amdhsa_exception_int_div_zero 0
	.end_amdhsa_kernel

amdhsa.kernels:
  - .agpr_count:     16
    .args:
      - .actual_access:  read_only
        .address_space:  global
        .offset:         0
        .size:           8
        .value_kind:     global_buffer
      - .actual_access:  read_only
        .address_space:  global
        .offset:         8
        .size:           8
        .value_kind:     global_buffer
      - .actual_access:  read_only
        .address_space:  global
        .offset:         16
        .size:           8
        .value_kind:     global_buffer
      - .actual_access:  read_only
        .address_space:  global
        .offset:         24
        .size:           8
        .value_kind:     global_buffer
      - .actual_access:  write_only
        .address_space:  global
        .offset:         32
        .size:           8
        .value_kind:     global_buffer
      - .actual_access:  write_only
        .address_space:  global
        .offset:         40
        .size:           8
        .value_kind:     global_buffer
      - .actual_access:  read_only
        .address_space:  global
        .offset:         48
        .size:           8
        .value_kind:     global_buffer
      - .actual_access:  read_only
        .address_space:  global
        .offset:         56
        .size:           8
        .value_kind:     global_buffer
      - .actual_access:  read_only
        .address_space:  global
        .offset:         64
        .size:           8
        .value_kind:     global_buffer
      - .actual_access:  read_only
        .address_space:  global
        .offset:         72
        .size:           8
        .value_kind:     global_buffer
      - .actual_access:  read_only
        .address_space:  global
        .offset:         80
        .size:           8
        .value_kind:     global_buffer
      - .actual_access:  write_only
        .address_space:  global
        .offset:         88
        .size:           8
        .value_kind:     global_buffer
      - .actual_access:  write_only
        .address_space:  global
        .offset:         96
        .size:           8
        .value_kind:     global_buffer
    .group_segment_fixed_size: 40960
    .kernarg_segment_align: 8
    .kernarg_segment_size: 104
    .language:       OpenCL C
    .language_version:
      - 2
      - 0
    .max_flat_workgroup_size: 256
    .name:           _Z5k_triPKfS0_S0_S0_PDF16_S1_S0_S0_S0_S0_S0_S1_S1_
    .private_segment_fixed_size: 0
    .sgpr_count:     33
    .sgpr_spill_count: 0
    .symbol:         _Z5k_triPKfS0_S0_S0_PDF16_S1_S0_S0_S0_S0_S0_S1_S1_.kd
    .uniform_work_group_size: 1
    .uses_dynamic_stack: false
    .vgpr_count:     248
    .vgpr_spill_count: 0
    .wavefront_size: 64
  - .agpr_count:     0
    .args:
      - .actual_access:  read_only
        .address_space:  global
        .offset:         0
        .size:           8
        .value_kind:     global_buffer
      - .address_space:  global
        .offset:         8
        .size:           8
        .value_kind:     global_buffer
      - .address_space:  global
        .offset:         16
        .size:           8
        .value_kind:     global_buffer
      - .actual_access:  read_only
        .address_space:  global
        .offset:         24
        .size:           8
        .value_kind:     global_buffer
      - .actual_access:  read_only
        .address_space:  global
        .offset:         32
        .size:           8
        .value_kind:     global_buffer
      - .actual_access:  read_only
        .address_space:  global
        .offset:         40
        .size:           8
        .value_kind:     global_buffer
      - .actual_access:  read_only
        .address_space:  global
        .offset:         48
        .size:           8
        .value_kind:     global_buffer
      - .actual_access:  write_only
        .address_space:  global
        .offset:         56
        .size:           8
        .value_kind:     global_buffer
    .group_segment_fixed_size: 132096
    .kernarg_segment_align: 8
    .kernarg_segment_size: 64
    .language:       OpenCL C
    .language_version:
      - 2
      - 0
    .max_flat_workgroup_size: 512
    .name:           _Z7k_fusedPKDF16_S0_S0_S0_PKfS2_S2_Pf
    .private_segment_fixed_size: 0
    .sgpr_count:     64
    .sgpr_spill_count: 0
    .symbol:         _Z7k_fusedPKDF16_S0_S0_S0_PKfS2_S2_Pf.kd
    .uniform_work_group_size: 1
    .uses_dynamic_stack: false
    .vgpr_count:     256
    .vgpr_spill_count: 0
    .wavefront_size: 64
